# stacked: + head-norm DPP sums, conv/SiLU v_cvt_pk packing, nt on scan V loads
# speedup vs baseline: 1.0069x; 1.0069x over previous
; __device__ __forceinline__ void p4_scan(const Args& a, const Frame& F) {
;     ...
;             auto prefetch = [&](int ci) {
;                 const int base = chunk_base(ci);
; #pragma unroll
;                 for (int i = 0; i < 8; ++i) { const int p = ht + 256 * i, row = p >> 4, c16 = p & 15; const int tok = base + (dir ? 127 - row : row);
;                     pq[i] = *(const u32x4*)(QKC + (size_t)tok * 1024 + h * 128 + c16 * 8); pk[i] = *(const u32x4*)(QKC + (size_t)tok * 1024 + 512 + h * 128 + c16 * 8); }
; #pragma unroll
;                 for (int i = 0; i < 2; ++i) { const int p = ht + 256 * i, row = p >> 2, cc = p & 3; const int tok = base + (dir ? 127 - row : row);
;                     pv[i] = *(const u32x4*)(PV + (size_t)tok * 512 + h * 128 + vs * 32 + cc * 8); pga[i] = GS[(size_t)hd * TA + tok]; }
; #pragma unroll
;                 for (int i = 0; i < 2; ++i) { const int idx = ht + 256 * i; if (idx < 384) { const int row = idx & 127, arr = idx >> 7; const int tok = base + (dir ? 127 - row : row); pgl[i] = GS[(size_t)(arr * 8 + hd) * TA + tok]; } }
;                 pbt = CH[(hd * 528 + (base >> 7)) * 2]; ppx = CH[(hd * 528 + (base >> 7)) * 2 + 1];
.LBB0_492:
	s_waitcnt vmcnt(16)
	s_add_i32 s35, s44, 1
	s_cmpk_eq_i32 s44, 0x41
	s_cselect_b32 s56, s44, s35
	s_sub_i32 s58, 0x41, s56
	v_sub_co_u32_e64 v8, s[54:55], s56, 2
	s_and_b64 s[56:57], s[4:5], exec
	v_readfirstlane_b32 s56, v8
	s_cselect_b32 s56, s56, s58
	s_lshl_b32 s56, s56, 7
	s_add_i32 s56, s56, s33
	s_and_b64 s[54:55], s[54:55], exec
	s_cselect_b32 s56, s34, s56
	v_add_u32_e32 v8, s56, v104
	v_ashrrev_i32_e32 v9, 31, v8
	v_lshlrev_b64 v[10:11], 10, v[8:9]
	v_lshl_add_u64 v[10:11], v[86:87], 0, v[10:11]
	v_lshl_add_u64 v[8:9], v[8:9], 2, s[50:51]
	global_load_dwordx4 v[12:15], v[10:11], off nt
	global_load_dword v172, v[8:9], off
	v_add_u32_e32 v8, s56, v105
	v_ashrrev_i32_e32 v9, 31, v8
	v_lshlrev_b64 v[10:11], 10, v[8:9]
	v_lshl_add_u64 v[10:11], v[86:87], 0, v[10:11]
	v_lshl_add_u64 v[94:95], v[8:9], 2, s[50:51]
	global_load_dwordx4 v[8:11], v[10:11], off nt
	s_nop 0
	global_load_dword v171, v[94:95], off
	v_or_b32_e32 v94, s56, v106
	v_ashrrev_i32_e32 v95, 31, v94
	s_and_saveexec_b64 s[54:55], s[6:7]
	s_cbranch_execz .LBB0_494
	v_lshl_add_u64 v[190:191], v[94:95], 2, v[88:89]
	global_load_dword v108, v[190:191], off
